# baseline (speedup 1.0000x reference)
.Ll1g_done:
	s_cmp_gt_i32 s3, 30
	s_cbranch_scc1 .Ll1g_keep
	s_setprio 0
.Ll1g_keep:
	v_add_u32_e32 v6, v70, v71
	s_nop 4
	v_cvt_pk_f16_f32 v2, v18, v22
	v_cvt_pk_f16_f32 v3, v26, v30
	v_cvt_pk_f16_f32 v4, v34, v38
	v_cvt_pk_f16_f32 v5, v42, v46
	ds_write_b128 v6, v[2:5]
	v_cvt_pk_f16_f32 v2, v19, v23
	v_cvt_pk_f16_f32 v3, v27, v31
	v_cvt_pk_f16_f32 v4, v35, v39
	v_cvt_pk_f16_f32 v5, v43, v47
	ds_write_b128 v6, v[2:5] offset:256
	v_cvt_pk_f16_f32 v2, v20, v24
	v_cvt_pk_f16_f32 v3, v28, v32
	v_cvt_pk_f16_f32 v4, v36, v40
	v_cvt_pk_f16_f32 v5, v44, v48
	ds_write_b128 v6, v[2:5] offset:512
	v_cvt_pk_f16_f32 v2, v21, v25
	v_cvt_pk_f16_f32 v3, v29, v33
	v_cvt_pk_f16_f32 v4, v37, v41
	v_cvt_pk_f16_f32 v5, v45, v49
	ds_write_b128 v6, v[2:5] offset:768

.LBB2_57:
	s_endpgm
	s_nop 0
	s_nop 0
	s_nop 0
	s_nop 0
	s_nop 0
	s_nop 0
	s_nop 0
	s_nop 0
	s_nop 0
	s_nop 0
	s_nop 0
	s_nop 0
	s_endpgm
